# prep kernel stores written through (sc0 sc1) so the kernel boundary has no dirty lines to write back
# baseline (speedup 1.0000x reference)
_Z11prep_kernelPKfS0_PfPDv4_DF16_:
	s_load_dwordx4 s[4:7], s[0:1], 0x0
	s_load_dwordx4 s[8:11], s[0:1], 0x10
	s_lshl_b32 s2, s2, 8
	v_add_u32_e32 v2, s2, v0
	v_lshrrev_b32_e32 v12, 5, v2
	s_movk_i32 s3, 0x2710
	v_cmp_gt_u32_e32 vcc, s3, v12
	s_and_saveexec_b64 s[12:13], vcc
	s_cbranch_execz .Lprep_end
	v_and_b32_e32 v14, 31, v2
	v_lshlrev_b32_e32 v1, 4, v14
	v_lshlrev_b32_e32 v3, 4, v2
	s_waitcnt lgkmcnt(0)
	global_load_dwordx4 v[4:7], v1, s[6:7]
	global_load_dwordx4 v[8:11], v3, s[4:5]
	v_lshlrev_b32_e32 v13, 3, v2
	v_lshlrev_b32_e32 v15, 2, v12
	s_waitcnt vmcnt(0)
	v_mul_f32_e32 v5, v9, v5
	v_fmac_f32_e32 v5, v8, v4
	v_fmac_f32_e32 v5, v10, v6
	v_fmac_f32_e32 v5, v11, v7
	v_cvt_pk_f16_f32 v6, v8, v9
	v_cvt_pk_f16_f32 v7, v10, v11
	global_store_dwordx2 v13, v[6:7], s[10:11] sc0 sc1
	v_add_f32_dpp v5, v5, v5 quad_perm:[1,0,3,2] row_mask:0xf bank_mask:0xf
	s_nop 1
	v_add_f32_dpp v5, v5, v5 quad_perm:[2,3,0,1] row_mask:0xf bank_mask:0xf
	s_nop 1
	v_add_f32_dpp v5, v5, v5 row_half_mirror row_mask:0xf bank_mask:0xf
	s_nop 1
	v_add_f32_dpp v5, v5, v5 row_mirror row_mask:0xf bank_mask:0xf
	s_nop 1
	v_add_f32_dpp v5, v5, v5 row_bcast:15 row_mask:0xa bank_mask:0xf
	v_cmp_eq_u32_e32 vcc, 16, v14
	s_and_b64 exec, exec, vcc
	global_store_dword v15, v5, s[8:9] sc0 sc1
